# RowExch partial-sum stores without sc1 when the partner workgroups share the XCC (F.loc); sc1 kept otherwise
# baseline (speedup 1.0000x reference)
;     __device__ __forceinline__ bool run(const f32x4 (&v)[2][2][4][2], const Unit& u, int wr, int wc, int fr, int fq, PG8_LAS unsigned char* lds, int wid, int lane) const {
;     ...
;         asm volatile("s_waitcnt lgkmcnt(0)" ::: "memory"); __builtin_amdgcn_s_barrier(); asm volatile("" ::: "memory");
;         const int row = wid * 32 + (lane & 31);
;         if (lane < 32) { const float t = (P[row * 4 + 0] + P[row * 4 + 1]) + (P[row * 4 + 2] + P[row * 4 + 3]);
;             __hip_atomic_store((unsigned*)xbuf + ((size_t)(pm * BM + row) * 4 + pn), __float_as_uint(t), __ATOMIC_RELAXED, __HIP_MEMORY_SCOPE_AGENT); }
;         asm volatile("s_waitcnt vmcnt(0)" ::: "memory");
;         if (lane == 0) __hip_atomic_fetch_add(cnt + 64 * pm, 1u, __ATOMIC_RELAXED, __HIP_MEMORY_SCOPE_AGENT);
.LBB0_682:
	s_or_b64 exec, exec, s[6:7]
	s_add_u32 s6, s78, 0x190000
	s_addc_u32 s7, s79, 0
	s_lshr_b32 s8, s8, 24
	s_lshl_b32 s5, s96, 5
	s_add_i32 s8, s3, s8
	s_waitcnt lgkmcnt(0)
	s_barrier
	s_ashr_i32 s16, s8, 8
	v_and_or_b32 v4, v187, 31, s5
	v_cmp_gt_i32_e64 s[8:9], 32, v187
	v_lshl_add_u32 v0, s16, 8, v4
	s_and_saveexec_b64 s[10:11], s[8:9]
	s_cbranch_execz .LBB0_684
	v_lshl_add_u32 v1, v4, 4, 0
	ds_read_b128 v[6:9], v1
	v_ashrrev_i32_e32 v1, 31, v0
	s_ashr_i32 s5, s4, 31
	s_waitcnt lgkmcnt(0)
	v_mov_b32_e32 v2, v7
	v_mov_b32_e32 v3, v8
	v_mov_b32_e32 v7, v9
	v_pk_add_f32 v[2:3], v[2:3], v[6:7]
	v_lshl_add_u64 v[6:7], v[0:1], 4, s[6:7]
	v_pk_add_f32 v[2:3], v[2:3], v[2:3] op_sel:[0,1] op_sel_hi:[1,0]
	v_lshl_add_u64 v[6:7], s[4:5], 2, v[6:7]
	v_readlane_b32 s100, v254, 24
	s_cmp_lg_u32 s100, 0
	s_cbranch_scc1 .Lmy_rx1_loc
	global_store_dword v[6:7], v2, off sc1
	s_branch .Lmy_rx1_done
.Lmy_rx1_loc:
	global_store_dword v[6:7], v2, off
.Lmy_rx1_done:
.LBB0_684:
	s_or_b64 exec, exec, s[10:11]
	s_waitcnt vmcnt(0)
	s_add_u32 s17, s78, 0x20000
	s_addc_u32 s20, s79, 0
	v_cmp_ne_u32_e64 s[12:13], 0, v187
	v_cmp_eq_u32_e64 s[10:11], 0, v187
	s_and_saveexec_b64 s[4:5], s[10:11]
	s_cbranch_execz .LBB0_687
	s_mov_b64 s[14:15], exec
	v_mbcnt_lo_u32_b32 v1, s14, 0
	v_mbcnt_hi_u32_b32 v1, s15, v1
	v_cmp_eq_u32_e32 vcc, 0, v1
	s_and_b64 s[22:23], exec, vcc
	s_mov_b64 exec, s[22:23]
	s_cbranch_execz .LBB0_687
	s_lshl_b32 s22, s16, 6
	s_ashr_i32 s23, s22, 31
	s_lshl_b64 s[22:23], s[22:23], 2
	s_add_u32 s22, s17, s22
	s_addc_u32 s23, s20, s23
	s_bcnt1_i32_b64 s14, s[14:15]
	v_mov_b32_e32 v1, 0
	s_waitcnt lgkmcnt(0)
	v_mov_b32_e32 v2, s14
	global_atomic_add v1, v2, s[22:23]

;     __device__ __forceinline__ bool run(const f32x4 (&v)[2][2][4][2], const Unit& u, int wr, int wc, int fr, int fq, PG8_LAS unsigned char* lds, int wid, int lane) const {
;     ...
;         const int row = wid * 32 + (lane & 31);
;         if (lane < 32) { const float t = (P[row * 4 + 0] + P[row * 4 + 1]) + (P[row * 4 + 2] + P[row * 4 + 3]);
;             __hip_atomic_store((unsigned*)xbuf + ((size_t)(pm * BM + row) * 4 + pn), __float_as_uint(t), __ATOMIC_RELAXED, __HIP_MEMORY_SCOPE_AGENT); }
.LBB0_999:
	s_or_b64 exec, exec, s[6:7]
	s_add_u32 s6, s78, 0x190000
	s_addc_u32 s7, s79, 0
	s_lshr_b32 s8, s8, 24
	s_lshl_b32 s5, s96, 5
	s_add_i32 s3, s3, s8
	s_waitcnt lgkmcnt(0)
	s_barrier
	s_ashr_i32 s3, s3, 8
	v_and_or_b32 v4, v203, 31, s5
	v_cmp_gt_i32_e64 s[8:9], 32, v203
	v_lshl_add_u32 v0, s3, 8, v4
	s_and_saveexec_b64 s[10:11], s[8:9]
	s_cbranch_execz .LBB0_1001
	v_lshl_add_u32 v1, v4, 4, 0
	ds_read_b128 v[6:9], v1
	v_ashrrev_i32_e32 v1, 31, v0
	s_ashr_i32 s5, s4, 31
	s_waitcnt lgkmcnt(0)
	v_mov_b32_e32 v2, v7
	v_mov_b32_e32 v3, v8
	v_mov_b32_e32 v7, v9
	v_pk_add_f32 v[2:3], v[2:3], v[6:7]
	v_lshl_add_u64 v[6:7], v[0:1], 4, s[6:7]
	v_pk_add_f32 v[2:3], v[2:3], v[2:3] op_sel:[0,1] op_sel_hi:[1,0]
	v_lshl_add_u64 v[6:7], s[4:5], 2, v[6:7]
	v_readlane_b32 s100, v254, 24
	s_cmp_lg_u32 s100, 0
	s_cbranch_scc1 .Lmy_rx0_loc
	global_store_dword v[6:7], v2, off sc1
	s_branch .Lmy_rx0_done

;     __device__ __forceinline__ bool run(const f32x4 (&v)[2][2][4][2], const Unit& u, int wr, int wc, int fr, int fq, PG8_LAS unsigned char* lds, int wid, int lane) const {
;     ...
;         asm volatile("s_waitcnt vmcnt(0)" ::: "memory");
;         if (lane == 0) __hip_atomic_fetch_add(cnt + 64 * pm, 1u, __ATOMIC_RELAXED, __HIP_MEMORY_SCOPE_AGENT);
.Lmy_rx0_done:
.LBB0_1001:
	s_or_b64 exec, exec, s[10:11]
	s_waitcnt vmcnt(0)
	s_add_u32 s16, s78, 0x28000
	s_addc_u32 s17, s79, 0
	v_cmp_ne_u32_e64 s[12:13], 0, v203
	v_cmp_eq_u32_e64 s[10:11], 0, v203
	s_and_saveexec_b64 s[4:5], s[10:11]
	s_cbranch_execz .LBB0_1004
	s_mov_b64 s[14:15], exec
	v_mbcnt_lo_u32_b32 v1, s14, 0
	v_mbcnt_hi_u32_b32 v1, s15, v1
	v_cmp_eq_u32_e32 vcc, 0, v1
	s_and_b64 s[24:25], exec, vcc
	s_mov_b64 exec, s[24:25]
	s_cbranch_execz .LBB0_1004
	s_lshl_b32 s24, s3, 6
	s_ashr_i32 s25, s24, 31
	s_lshl_b64 s[24:25], s[24:25], 2
	s_add_u32 s24, s16, s24
	s_addc_u32 s25, s17, s25
	s_bcnt1_i32_b64 s14, s[14:15]
	v_mov_b32_e32 v1, 0
	s_waitcnt lgkmcnt(0)
	v_mov_b32_e32 v2, s14
	global_atomic_add v1, v2, s[24:25]
